# v39 + static s_setprio 1 for the older wave half (waves 0-3) at attention / retention phase entry (the other half was tried before)
# baseline (speedup 1.0000x reference)
.LBB0_677:
	s_cmp_gt_u32 s88, 3
	s_cbranch_scc1 .Lprio_o0
	s_setprio 1
